# P0 weight-conversion queue: ticket atomic return no longer waited in-loop (consumed one iteration later)
# speedup vs baseline: 1.0088x; 1.0088x over previous
; #define LAS __attribute__((address_space(3)))
; __device__ __forceinline__ unsigned xb_add(unsigned* p, unsigned v) { return __hip_atomic_fetch_add(p, v, __ATOMIC_RELAXED, __HIP_MEMORY_SCOPE_AGENT); }
; __device__ __forceinline__ void phase_prologue(const Args& a, LAS unsigned char* lds) {
;     ...
;     unsigned* cq_head = (unsigned*)(a.ws + WS_CTL) + 8192 + 768;
;     volatile LAS int* qs = (volatile LAS int*)(lds + 128 * 129 * 4);
;     int pend = 0, it = 0;
;     if (tid == 0) { qs[0] = (int)xb_add(cq_head, 1u); pend = (int)xb_add(cq_head, 1u); }
;     __syncthreads();
;     for (int u = qs[0]; u < CTOT; u = qs[it & 1]) {
;         int r = u; const float* src; int ldn, nvalid, NT, mode = 0; bf16_t* dst;
;         if (r < CJ0) { src = a.in[I_EVIN]; ldn = 6144; nvalid = 6144; NT = 48; dst = (bf16_t*)(a.ws + WS_WIN0); }
.LBB0_36:
	s_or_b64 exec, exec, s[12:13]
	s_waitcnt vmcnt(0)
	v_readfirstlane_b32 s8, v2
	s_nop 1
	v_add_u32_e32 v1, s8, v1
	v_mov_b32_e32 v252, v1
.LBB0_37:
	s_or_b64 exec, exec, s[6:7]
	s_add_i32 s6, 0, 0x10200
	v_mov_b32_e32 v2, s6
	s_waitcnt lgkmcnt(0)
	s_barrier
	ds_read_b32 v2, v2
	s_movk_i32 s6, 0x481f
	s_waitcnt lgkmcnt(0)
	v_cmp_lt_i32_e32 vcc, s6, v2
	v_readfirstlane_b32 s20, v2
	s_cbranch_vccnz .LBB0_79
	v_lshlrev_b32_e32 v2, 3, v0
	v_or_b32_e32 v6, 0xa00, v0
	v_and_b32_e32 v2, 0x78, v2
	s_movk_i32 s6, 0x204
	v_or_b32_e32 v4, 0x200, v0
	v_or_b32_e32 v5, 0x600, v0
	v_lshrrev_b32_e32 v40, 5, v6
	v_or_b32_e32 v6, 0xe00, v0
	v_or_b32_e32 v8, 0x400, v0
	v_mad_u32_u24 v3, v2, s6, 0
	v_lshrrev_b32_e32 v38, 5, v4
	v_lshrrev_b32_e32 v39, 5, v5
	v_lshrrev_b32_e32 v41, 5, v6
	v_lshrrev_b32_e32 v9, 5, v8
	v_lshrrev_b32_e32 v42, 4, v0
	v_lshrrev_b32_e32 v44, 4, v4
	v_lshrrev_b32_e32 v46, 4, v8
	v_lshrrev_b32_e32 v48, 4, v5
	v_mul_u32_u24_e32 v6, 0x204, v104
	v_mul_u32_u24_e32 v7, 0x204, v38
	v_mul_u32_u24_e32 v9, 0x204, v9
	v_mul_u32_u24_e32 v10, 0x204, v39
	v_mul_u32_u24_e32 v11, 0x204, v40
	v_lshl_add_u32 v43, v42, 2, v3
	v_lshl_add_u32 v45, v44, 2, v3
	v_lshl_add_u32 v47, v46, 2, v3
	v_lshl_add_u32 v49, v48, 2, v3
	v_mul_u32_u24_e32 v3, 0x204, v41
	v_mov_b32_e32 v35, 0
	v_or_b32_e32 v50, 32, v104
	v_or_b32_e32 v51, 64, v104
	v_or_b32_e32 v52, 0x60, v104
	s_mov_b32 s16, 1
	v_add_u32_e32 v53, v106, v6
	v_add_u32_e32 v54, v106, v7
	v_add_u32_e32 v55, v106, v9
	v_add_u32_e32 v56, v106, v10
	v_add_u32_e32 v57, v106, v11
	v_add_u32_e32 v58, v106, v3
	v_lshlrev_b32_e32 v34, 1, v2
	s_movk_i32 s17, 0x4820
	s_branch .LBB0_41
.LBB0_40:
	s_or_b64 exec, exec, s[6:7]
	s_lshl_b32 s6, s14, 2
	s_add_i32 s6, s6, 0
	s_add_i32 s6, s6, 0x10200
	s_waitcnt lgkmcnt(0)
	s_barrier
	v_mov_b32_e32 v2, s6
	ds_read_b32 v2, v2
	s_add_i32 s16, s16, 1
	s_waitcnt lgkmcnt(0)
	v_cmp_gt_i32_e32 vcc, s17, v2
	v_readfirstlane_b32 s20, v2
	s_cbranch_vccz .LBB0_79

; #define LAS __attribute__((address_space(3)))
; __device__ __forceinline__ void lds_barrier() { asm volatile("s_waitcnt lgkmcnt(0)" ::: "memory"); __builtin_amdgcn_s_barrier(); asm volatile("" ::: "memory"); }
; __device__ __forceinline__ unsigned xb_add(unsigned* p, unsigned v) { return __hip_atomic_fetch_add(p, v, __ATOMIC_RELAXED, __HIP_MEMORY_SCOPE_AGENT); }
; __device__ __forceinline__ void phase_prologue(const Args& a, LAS unsigned char* lds) {
;     ...
;         for (int i = 0; i < 8; ++i) { const int id = tid + 512 * i, row = id >> 5, c4 = id & 31;
;             LAS float* tp = tile + row * 129 + c4 * 4; tp[0] = v[i][0]; tp[1] = v[i][1]; tp[2] = v[i][2]; tp[3] = v[i][3]; }
;         lds_barrier();
; #pragma unroll
;         for (int i = 0; i < 4; ++i) { const int piece = tid + 512 * i, nl = piece >> 4, kg = piece & 15; const LAS float* s = tile + (kg * 8) * 129 + nl;
;             u32x4 o; o.x = pk2(s[0], s[129]); o.y = pk2(s[258], s[387]); o.z = pk2(s[516], s[645]); o.w = pk2(s[774], s[903]);
;             *(u32x4*)(dst + (size_t)(drow0 + nl) * 2048 + k0 + kg * 8) = o; }
;         ++it;
;         if (tid == 0) { qs[it & 1] = pend; pend = (int)xb_add(cq_head, 1u); }
;         lds_barrier();
;     }
.LBB0_76:
	s_or_b64 exec, exec, s[14:15]
	s_waitcnt vmcnt(0)
	ds_write2_b32 v53, v6, v7 offset1:1
	ds_write2_b32 v53, v8, v9 offset0:2 offset1:3
	ds_write2_b32 v54, v2, v3 offset1:1
	ds_write2_b32 v54, v4, v5 offset0:2 offset1:3
	ds_write2_b32 v55, v14, v15 offset1:1
	ds_write2_b32 v55, v16, v17 offset0:2 offset1:3
	ds_write2_b32 v56, v10, v11 offset1:1
	ds_write2_b32 v56, v12, v13 offset0:2 offset1:3
	v_add_u32_e32 v2, 0x8100, v53
	ds_write2_b32 v2, v22, v23 offset1:1
	v_add_u32_e32 v2, 0x8108, v53
	ds_write2_b32 v2, v24, v25 offset1:1
	ds_write2_b32 v57, v18, v19 offset1:1
	ds_write2_b32 v57, v20, v21 offset0:2 offset1:3
	v_add_u32_e32 v2, 0xc180, v53
	ds_write2_b32 v2, v30, v31 offset1:1
	v_add_u32_e32 v2, 0xc188, v53
	ds_write2_b32 v2, v32, v33 offset1:1
	ds_write2_b32 v58, v26, v27 offset1:1
	ds_write2_b32 v58, v28, v29 offset0:2 offset1:3
	s_waitcnt lgkmcnt(0)
	s_barrier
	v_add_u32_e32 v4, 0x400, v43
	v_add_u32_e32 v6, 0x800, v43
	s_lshl_b32 s14, s20, 8
	ds_read2_b32 v[2:3], v43 offset1:129
	ds_read2_b32 v[4:5], v4 offset0:2 offset1:131
	ds_read2_b32 v[6:7], v6 offset0:4 offset1:133
	v_add_u32_e32 v8, 0xc00, v43
	s_or_b32 s14, s14, s18
	ds_read2_b32 v[8:9], v8 offset0:6 offset1:135
	s_and_b64 s[8:9], s[8:9], exec
	s_cselect_b32 s14, s13, s14
	s_ashr_i32 s13, s12, 31
	v_add_u32_e32 v12, 0x400, v45
	v_add_u32_e32 v14, 0x800, v45
	v_add_u32_e32 v16, 0xc00, v45
	s_lshl_b64 s[8:9], s[12:13], 1
	ds_read2_b32 v[12:13], v12 offset0:2 offset1:131
	ds_read2_b32 v[14:15], v14 offset0:4 offset1:133
	ds_read2_b32 v[16:17], v16 offset0:6 offset1:135
	s_add_u32 s6, s6, s8
	s_waitcnt lgkmcnt(6)
	v_cvt_pk_bf16_f32 v2, v2, v3
	s_waitcnt lgkmcnt(5)
	v_cvt_pk_bf16_f32 v3, v4, v5
	s_waitcnt lgkmcnt(4)
	v_cvt_pk_bf16_f32 v4, v6, v7
	v_or_b32_e32 v6, s14, v42
	s_addc_u32 s7, s7, s9
	s_waitcnt lgkmcnt(3)
	v_cvt_pk_bf16_f32 v5, v8, v9
	v_ashrrev_i32_e32 v7, 31, v6
	ds_read2_b32 v[8:9], v45 offset1:129
	v_lshl_add_u64 v[10:11], s[6:7], 0, v[34:35]
	v_lshlrev_b64 v[6:7], 12, v[6:7]
	v_lshl_add_u64 v[6:7], v[10:11], 0, v[6:7]
	global_store_dwordx4 v[6:7], v[2:5], off
	v_or_b32_e32 v6, s14, v44
	v_ashrrev_i32_e32 v7, 31, v6
	s_waitcnt lgkmcnt(3)
	v_cvt_pk_bf16_f32 v3, v12, v13
	s_waitcnt lgkmcnt(2)
	v_cvt_pk_bf16_f32 v4, v14, v15
	s_waitcnt lgkmcnt(1)
	v_cvt_pk_bf16_f32 v5, v16, v17
	v_add_u32_e32 v12, 0x400, v47
	v_add_u32_e32 v14, 0x800, v47
	v_add_u32_e32 v16, 0xc00, v47
	ds_read2_b32 v[12:13], v12 offset0:2 offset1:131
	ds_read2_b32 v[14:15], v14 offset0:4 offset1:133
	ds_read2_b32 v[16:17], v16 offset0:6 offset1:135
	s_waitcnt lgkmcnt(3)
	v_cvt_pk_bf16_f32 v2, v8, v9
	ds_read2_b32 v[8:9], v47 offset1:129
	v_lshlrev_b64 v[6:7], 12, v[6:7]
	v_lshl_add_u64 v[6:7], v[10:11], 0, v[6:7]
	global_store_dwordx4 v[6:7], v[2:5], off
	v_or_b32_e32 v6, s14, v46
	v_ashrrev_i32_e32 v7, 31, v6
	s_waitcnt lgkmcnt(3)
	v_cvt_pk_bf16_f32 v3, v12, v13
	s_waitcnt lgkmcnt(2)
	v_cvt_pk_bf16_f32 v4, v14, v15
	s_waitcnt lgkmcnt(1)
	v_cvt_pk_bf16_f32 v5, v16, v17
	v_add_u32_e32 v12, 0x400, v49
	v_add_u32_e32 v14, 0x800, v49
	v_add_u32_e32 v16, 0xc00, v49
	s_waitcnt lgkmcnt(0)
	v_cvt_pk_bf16_f32 v2, v8, v9
	v_lshlrev_b64 v[6:7], 12, v[6:7]
	ds_read2_b32 v[8:9], v49 offset1:129
	ds_read2_b32 v[12:13], v12 offset0:2 offset1:131
	ds_read2_b32 v[14:15], v14 offset0:4 offset1:133
	ds_read2_b32 v[16:17], v16 offset0:6 offset1:135
	v_lshl_add_u64 v[6:7], v[10:11], 0, v[6:7]
	global_store_dwordx4 v[6:7], v[2:5], off
	v_add_u32_e32 v6, s14, v48
	v_ashrrev_i32_e32 v7, 31, v6
	v_lshlrev_b64 v[6:7], 12, v[6:7]
	s_waitcnt lgkmcnt(3)
	v_cvt_pk_bf16_f32 v2, v8, v9
	s_waitcnt lgkmcnt(2)
	v_cvt_pk_bf16_f32 v3, v12, v13
	s_waitcnt lgkmcnt(1)
	v_cvt_pk_bf16_f32 v4, v14, v15
	s_waitcnt lgkmcnt(0)
	v_cvt_pk_bf16_f32 v5, v16, v17
	v_lshl_add_u64 v[6:7], v[10:11], 0, v[6:7]
	s_and_b32 s14, s16, 1
	global_store_dwordx4 v[6:7], v[2:5], off
	s_and_saveexec_b64 s[6:7], s[0:1]
	s_cbranch_execz .LBB0_40
	s_lshl_b32 s12, s14, 2
	s_add_i32 s12, s12, 0
	s_add_i32 s12, s12, 0x10200
	v_mov_b32_e32 v2, s12
	ds_write_b32 v2, v252
	v_mov_b32_e32 v2, 1
	s_nop 0
	global_atomic_add v252, v35, v2, s[4:5] sc0
	s_branch .LBB0_40
.LBB0_79:
	s_waitcnt vmcnt(0)
	v_readlane_b32 s0, v254, 0
	v_readlane_b32 s1, v254, 1
	v_writelane_b32 v254, s36, 45
	s_cmp_gt_i32 s1, 1
	s_cselect_b64 s[0:1], -1, 0
	v_writelane_b32 v254, s37, 46
	v_writelane_b32 v254, s38, 47
	v_writelane_b32 v254, s39, 48
	v_writelane_b32 v254, s40, 49
	v_writelane_b32 v254, s41, 50
	v_writelane_b32 v254, s42, 51
	v_writelane_b32 v254, s43, 52
	v_writelane_b32 v254, s44, 53
	v_writelane_b32 v254, s45, 54
	v_writelane_b32 v254, s46, 55
	v_writelane_b32 v254, s47, 56
	v_writelane_b32 v254, s48, 57
	v_writelane_b32 v254, s49, 58
	s_and_b64 s[2:3], s[2:3], s[0:1]
	v_writelane_b32 v254, s50, 59
	s_andn2_b64 vcc, exec, s[2:3]
	v_writelane_b32 v254, s51, 60
	s_cbranch_vccnz .LBB0_129
	s_waitcnt vmcnt(0)
	v_cmp_eq_u32_e32 vcc, 0, v0
	s_barrier
	s_and_saveexec_b64 s[2:3], vcc
	s_cbranch_execz .LBB0_128
	s_add_i32 s4, 0, 0x23fc0
	v_mov_b32_e32 v1, s4
	s_waitcnt vmcnt(0) expcnt(0) lgkmcnt(0)
	ds_read_b32 v3, v1
	s_add_i32 s4, 0, 0x23fc4
	v_mov_b32_e32 v1, s4
	ds_read_b32 v1, v1
	s_waitcnt lgkmcnt(1)
	v_cmp_ne_u32_e32 vcc, 0, v3
	s_cbranch_vccnz .LBB0_96
	v_readlane_b32 s4, v254, 27
	v_readlane_b32 s5, v254, 28
	s_load_dwordx2 s[8:9], s[4:5], 0x4
	s_add_u32 s4, s94, 0x4200
	s_addc_u32 s5, s95, 0
	s_add_u32 s6, s94, 0x4400
	s_addc_u32 s7, s95, 0
	s_waitcnt lgkmcnt(0)
	s_mul_i32 s33, s8, s85
	s_add_u32 s8, s94, 0x4500
	s_mul_i32 s33, s33, s9
	s_addc_u32 s9, s95, 0
	s_add_u32 s12, s94, 0x4600
	s_addc_u32 s13, s95, 0
	s_add_u32 s14, s94, 0x4700
	s_addc_u32 s15, s95, 0
	s_add_u32 s16, s94, 0x4800
	s_addc_u32 s17, s95, 0
	s_add_u32 s18, s94, 0x4900
	s_addc_u32 s19, s95, 0
	s_add_u32 s20, s94, 0x4a00
	s_addc_u32 s21, s95, 0
	s_add_u32 s22, s94, 0x4b00
	s_addc_u32 s23, s95, 0
	s_add_u32 s24, s94, 0x4c00
	s_addc_u32 s25, s95, 0
	s_add_u32 s26, s94, 0x4d00
	s_addc_u32 s27, s95, 0
	s_add_u32 s30, s94, 0x4e00
	s_addc_u32 s31, s95, 0
	s_add_u32 s34, s94, 0x4f00
	s_addc_u32 s35, s95, 0
	s_add_u32 s36, s94, 0x5000
	s_addc_u32 s37, s95, 0
	s_add_u32 s38, s94, 0x5100
	s_addc_u32 s39, s95, 0
	s_add_u32 s40, s94, 0x5200
	s_addc_u32 s41, s95, 0
	s_add_u32 s42, s94, 0x5300
	s_addc_u32 s43, s95, 0
	s_mov_b32 s50, 1
	v_mov_b32_e32 v17, 0
	s_branch .LBB0_84
